# baseline (speedup 1.0000x reference)
.LBB4_4:
	s_load_dword s2, s[0:1], 0x18
	v_lshrrev_b32_e32 v6, 4, v0
	v_xor_b32_e32 v1, v6, v0
	v_lshlrev_b32_e32 v1, 3, v1
	v_and_b32_e32 v2, 56, v1
	v_lshrrev_b32_e32 v1, 3, v0
	s_waitcnt lgkmcnt(0)
	v_mad_u64_u32 v[4:5], s[0:1], v1, s2, v[2:3]
	v_or_b32_e32 v3, 0x200, v0
	v_lshrrev_b32_e32 v3, 3, v3
	s_lshl_b32 s10, s12, 7
	s_ashr_i32 s13, s2, 31
	v_mul_lo_u32 v3, v3, s2
	s_lshl_b32 s0, s2, 7
	v_add_lshl_u32 v2, v3, v2, 1
	v_add_lshl_u32 v3, v4, s0, 1
	s_mul_i32 s0, s10, s13
	s_mul_hi_u32 s1, s10, s2
	s_add_i32 s1, s1, s0
	s_mul_i32 s0, s10, s2
	s_mul_i32 s11, s3, 0xc0
	s_lshl_b64 s[0:1], s[0:1], 1
	v_lshlrev_b32_e32 v122, 4, v0
	v_lshlrev_b32_e32 v1, 1, v4
	s_add_u32 s0, s4, s0
	s_mul_i32 s3, s11, s13
	s_mul_hi_u32 s4, s11, s2
	v_add_u32_e32 v4, 0, v122
	s_addc_u32 s1, s5, s1
	s_add_i32 s3, s4, s3
	s_mul_i32 s2, s11, s2
	v_readfirstlane_b32 s13, v4
	v_add_u32_e32 v5, 0x2000, v4
	s_lshl_b64 s[2:3], s[2:3], 1
	s_mov_b32 m0, s13
	v_readfirstlane_b32 s4, v5
	v_add_u32_e32 v5, 0x4000, v4
	s_add_u32 s2, s6, s2
	global_load_lds_dwordx4 v1, s[0:1]
	s_mov_b32 m0, s4
	v_readfirstlane_b32 s5, v5
	v_add_u32_e32 v5, 0x6000, v4
	s_addc_u32 s3, s7, s3
	global_load_lds_dwordx4 v2, s[0:1]
	s_mov_b32 m0, s5
	v_readfirstlane_b32 s6, v5
	v_add_u32_e32 v5, 0x8000, v4
	global_load_lds_dwordx4 v1, s[2:3]
	s_mov_b32 m0, s6
	v_readfirstlane_b32 s7, v5
	v_add_u32_e32 v5, 0xa000, v4
	global_load_lds_dwordx4 v2, s[2:3]
	s_mov_b32 m0, s7
	s_add_u32 s16, s0, 0x80
	v_readfirstlane_b32 s18, v5
	v_add_u32_e32 v5, 0xc000, v4
	global_load_lds_dwordx4 v3, s[2:3]
	s_addc_u32 s17, s1, 0
	s_mov_b32 m0, s18
	v_readfirstlane_b32 s14, v5
	v_add_u32_e32 v5, 0xe000, v4
	s_add_u32 s20, s2, 0x80
	global_load_lds_dwordx4 v1, s[16:17]
	s_mov_b32 m0, s14
	v_readfirstlane_b32 s15, v5
	v_add_u32_e32 v5, 0x10000, v4
	s_addc_u32 s21, s3, 0
	global_load_lds_dwordx4 v2, s[16:17]
	s_mov_b32 m0, s15
	v_readfirstlane_b32 s16, v5
	v_add_u32_e32 v5, 0x12000, v4
	global_load_lds_dwordx4 v1, s[20:21]
	s_mov_b32 m0, s16
	v_readfirstlane_b32 s17, v5
	global_load_lds_dwordx4 v2, s[20:21]
	s_mov_b32 m0, s17
	v_add_u32_e32 v5, 0x14000, v4
	global_load_lds_dwordx4 v3, s[20:21]
	s_add_u32 s20, s0, 0x100
	v_readfirstlane_b32 s19, v5
	v_add_u32_e32 v5, 0x16000, v4
	s_addc_u32 s21, s1, 0
	s_mov_b32 m0, s19
	v_readfirstlane_b32 s19, v5
	v_add_u32_e32 v5, 0x18000, v4
	s_add_u32 s22, s2, 0x100
	global_load_lds_dwordx4 v1, s[20:21]
	s_mov_b32 m0, s19
	v_readfirstlane_b32 s19, v5
	v_add_u32_e32 v5, 0x1a000, v4
	s_addc_u32 s23, s3, 0
	global_load_lds_dwordx4 v2, s[20:21]
	s_mov_b32 m0, s19
	v_readfirstlane_b32 s19, v5
	v_add_u32_e32 v4, 0x1c000, v4
	global_load_lds_dwordx4 v1, s[22:23]
	s_mov_b32 m0, s19
	v_readfirstlane_b32 s19, v4
	global_load_lds_dwordx4 v2, s[22:23]
	s_mov_b32 m0, s19
	v_and_b32_e32 v8, 15, v0
	global_load_lds_dwordx4 v3, s[22:23]
	v_lshrrev_b32_e32 v11, 2, v0
	v_bfe_u32 v9, v0, 6, 2
	v_bfe_u32 v5, v0, 1, 3
	v_and_or_b32 v4, v11, 64, v8
	v_lshlrev_b32_e32 v123, 7, v4
	v_bitop3_b32 v4, v6, v5, 3 bitop3:0x6c
	v_mul_u32_u24_e32 v10, 48, v9
	v_lshlrev_b32_e32 v6, 4, v4
	v_or_b32_e32 v4, v10, v8
	v_lshlrev_b32_e32 v7, 7, v4
	v_add_u32_e32 v13, 0, v7
	s_waitcnt vmcnt(10)
	s_barrier
	v_add_u32_e32 v4, v13, v6
	ds_read_b128 v[14:17], v4 offset:16384
	v_add_u32_e32 v50, 0, v123
	v_add_u32_e32 v6, v50, v6
	ds_read_b128 v[18:21], v6
	ds_read_b128 v[22:25], v4 offset:18432
	ds_read_b128 v[26:29], v6 offset:2048
	ds_read_b128 v[30:33], v4 offset:20480
	ds_read_b128 v[42:45], v6 offset:4096
	ds_read_b128 v[46:49], v6 offset:6144
	v_bfe_u32 v12, v0, 4, 2
	v_bitop3_b32 v0, v12, v5, 4 bitop3:0x36
	v_lshlrev_b32_e32 v5, 4, v0
	s_add_i32 s19, 0, 0x14000
	v_add_u32_e32 v124, s19, v5
	s_waitcnt lgkmcnt(0)
	v_mfma_f32_16x16x32_f16 v[34:37], v[14:17], v[18:21], 0
	v_add_u32_e32 v7, v7, v124
	v_mfma_f32_16x16x32_f16 v[38:41], v[22:25], v[18:21], 0
	v_mfma_f32_16x16x32_f16 v[18:21], v[30:33], v[18:21], 0
	v_add_u32_e32 v0, v50, v5
	ds_read_b128 v[50:53], v0
	ds_read_b128 v[54:57], v0 offset:2048
	ds_read_b128 v[58:61], v0 offset:4096
	ds_read_b128 v[62:65], v0 offset:6144
	v_add_u32_e32 v5, v13, v5
	ds_read_b128 v[66:69], v5 offset:16384
	ds_read_b128 v[70:73], v5 offset:18432
	ds_read_b128 v[74:77], v5 offset:20480
	v_mfma_f32_16x16x32_f16 v[78:81], v[14:17], v[26:29], 0
	v_mfma_f32_16x16x32_f16 v[82:85], v[22:25], v[26:29], 0
	v_mfma_f32_16x16x32_f16 v[26:29], v[30:33], v[26:29], 0
	v_mfma_f32_16x16x32_f16 v[86:89], v[14:17], v[42:45], 0
	v_mfma_f32_16x16x32_f16 v[90:93], v[22:25], v[42:45], 0
	v_mfma_f32_16x16x32_f16 v[42:45], v[30:33], v[42:45], 0
	v_mfma_f32_16x16x32_f16 v[14:17], v[14:17], v[46:49], 0
	v_mfma_f32_16x16x32_f16 v[22:25], v[22:25], v[46:49], 0
	v_mfma_f32_16x16x32_f16 v[30:33], v[30:33], v[46:49], 0
	s_add_u32 s20, s0, 0x180
	s_mov_b32 m0, s13
	s_waitcnt vmcnt(5) lgkmcnt(0)
	s_barrier
	s_addc_u32 s21, s1, 0
	s_add_u32 s22, s2, 0x180
	s_addc_u32 s23, s3, 0
	s_waitcnt lgkmcnt(0)
	v_mfma_f32_16x16x32_f16 v[34:37], v[66:69], v[50:53], v[34:37]
	v_mfma_f32_16x16x32_f16 v[38:41], v[70:73], v[50:53], v[38:41]
	v_mfma_f32_16x16x32_f16 v[18:21], v[74:77], v[50:53], v[18:21]
	ds_read_b128 v[46:49], v6 offset:40960
	ds_read_b128 v[50:53], v6 offset:43008
	ds_read_b128 v[94:97], v6 offset:45056
	ds_read_b128 v[98:101], v6 offset:47104
	ds_read_b128 v[102:105], v4 offset:57344
	ds_read_b128 v[106:109], v4 offset:59392
	ds_read_b128 v[110:113], v4 offset:61440
	v_mfma_f32_16x16x32_f16 v[78:81], v[66:69], v[54:57], v[78:81]
	global_load_lds_dwordx4 v1, s[20:21]
	v_mfma_f32_16x16x32_f16 v[82:85], v[70:73], v[54:57], v[82:85]
	s_mov_b32 m0, s4
	s_nop 0
	global_load_lds_dwordx4 v2, s[20:21]
	v_mfma_f32_16x16x32_f16 v[26:29], v[74:77], v[54:57], v[26:29]
	s_mov_b32 m0, s5
	s_nop 0
	global_load_lds_dwordx4 v1, s[22:23]
	v_mfma_f32_16x16x32_f16 v[54:57], v[66:69], v[58:61], v[86:89]
	s_mov_b32 m0, s6
	s_nop 0
	global_load_lds_dwordx4 v2, s[22:23]
	v_mfma_f32_16x16x32_f16 v[86:89], v[70:73], v[58:61], v[90:93]
	s_mov_b32 m0, s7
	s_nop 0
	global_load_lds_dwordx4 v3, s[22:23]
	v_mfma_f32_16x16x32_f16 v[42:45], v[74:77], v[58:61], v[42:45]
	v_mfma_f32_16x16x32_f16 v[14:17], v[66:69], v[62:65], v[14:17]
	v_mfma_f32_16x16x32_f16 v[22:25], v[70:73], v[62:65], v[22:25]
	v_mfma_f32_16x16x32_f16 v[30:33], v[74:77], v[62:65], v[30:33]
	s_waitcnt lgkmcnt(0)
	v_mfma_f32_16x16x32_f16 v[34:37], v[102:105], v[46:49], v[34:37]
	v_mfma_f32_16x16x32_f16 v[38:41], v[106:109], v[46:49], v[38:41]
	v_mfma_f32_16x16x32_f16 v[18:21], v[110:113], v[46:49], v[18:21]
	ds_read_b128 v[46:49], v0 offset:40960
	ds_read_b128 v[58:61], v0 offset:43008
	ds_read_b128 v[62:65], v0 offset:45056
	ds_read_b128 v[66:69], v0 offset:47104
	ds_read_b128 v[70:73], v5 offset:57344
	ds_read_b128 v[74:77], v5 offset:59392
	ds_read_b128 v[90:93], v5 offset:61440
	v_mfma_f32_16x16x32_f16 v[78:81], v[102:105], v[50:53], v[78:81]
	v_mfma_f32_16x16x32_f16 v[82:85], v[106:109], v[50:53], v[82:85]
	v_mfma_f32_16x16x32_f16 v[26:29], v[110:113], v[50:53], v[26:29]
	v_mfma_f32_16x16x32_f16 v[50:53], v[102:105], v[94:97], v[54:57]
	v_mfma_f32_16x16x32_f16 v[54:57], v[106:109], v[94:97], v[86:89]
	v_mfma_f32_16x16x32_f16 v[42:45], v[110:113], v[94:97], v[42:45]
	v_mfma_f32_16x16x32_f16 v[86:89], v[102:105], v[98:101], v[14:17]
	v_mfma_f32_16x16x32_f16 v[22:25], v[106:109], v[98:101], v[22:25]
	v_mfma_f32_16x16x32_f16 v[30:33], v[110:113], v[98:101], v[30:33]
	s_add_u32 s20, s0, 0x200
	s_mov_b32 m0, s18
	s_waitcnt vmcnt(5) lgkmcnt(0)
	s_barrier
	s_addc_u32 s21, s1, 0
	s_add_u32 s22, s2, 0x200
	s_addc_u32 s23, s3, 0
	s_waitcnt lgkmcnt(0)
	v_mfma_f32_16x16x32_f16 v[34:37], v[70:73], v[46:49], v[34:37]
	v_mfma_f32_16x16x32_f16 v[38:41], v[74:77], v[46:49], v[38:41]
	v_mfma_f32_16x16x32_f16 v[46:49], v[90:93], v[46:49], v[18:21]
	v_add_u32_e32 v13, 0x14000, v6
	v_add_u32_e32 v15, 0x15000, v6
	s_nop 0
	v_add_u32_e32 v18, 0x18000, v4
	v_add_u32_e32 v14, 0x14800, v6
	ds_read_b128 v[94:97], v13
	ds_read_b128 v[98:101], v14
	v_add_u32_e32 v16, 0x15800, v6
	ds_read_b128 v[102:105], v15
	ds_read_b128 v[106:109], v16
	v_add_u32_e32 v19, 0x18800, v4
	ds_read_b128 v[110:113], v18
	ds_read_b128 v[114:117], v19
	v_add_u32_e32 v20, 0x19000, v4
	ds_read_b128 v[118:121], v20
	v_mfma_f32_16x16x32_f16 v[78:81], v[70:73], v[58:61], v[78:81]
	global_load_lds_dwordx4 v1, s[20:21]
	v_mfma_f32_16x16x32_f16 v[82:85], v[74:77], v[58:61], v[82:85]
	s_mov_b32 m0, s14
	s_nop 0
	global_load_lds_dwordx4 v2, s[20:21]
	v_mfma_f32_16x16x32_f16 v[26:29], v[90:93], v[58:61], v[26:29]
	s_mov_b32 m0, s15
	s_nop 0
	global_load_lds_dwordx4 v1, s[22:23]
	v_mfma_f32_16x16x32_f16 v[50:53], v[70:73], v[62:65], v[50:53]
	s_mov_b32 m0, s16
	s_nop 0
	global_load_lds_dwordx4 v2, s[22:23]
	v_mfma_f32_16x16x32_f16 v[54:57], v[74:77], v[62:65], v[54:57]
	s_mov_b32 m0, s17
	s_nop 0
	global_load_lds_dwordx4 v3, s[22:23]
	v_mfma_f32_16x16x32_f16 v[42:45], v[90:93], v[62:65], v[42:45]
	v_mfma_f32_16x16x32_f16 v[58:61], v[70:73], v[66:69], v[86:89]
	v_mfma_f32_16x16x32_f16 v[22:25], v[74:77], v[66:69], v[22:25]
	v_mfma_f32_16x16x32_f16 v[30:33], v[90:93], v[66:69], v[30:33]
	s_waitcnt lgkmcnt(0)
	v_mfma_f32_16x16x32_f16 v[34:37], v[110:113], v[94:97], v[34:37]
	v_mfma_f32_16x16x32_f16 v[38:41], v[114:117], v[94:97], v[38:41]
	v_mfma_f32_16x16x32_f16 v[46:49], v[118:121], v[94:97], v[46:49]
	v_add_u32_e32 v17, v124, v123
	ds_read_b128 v[62:65], v17 offset:2048
	ds_read_b128 v[66:69], v17 offset:4096
	ds_read_b128 v[70:73], v17 offset:6144
	ds_read_b128 v[74:77], v7 offset:16384
	ds_read_b128 v[86:89], v7 offset:18432
	ds_read_b128 v[90:93], v17
	ds_read_b128 v[94:97], v7 offset:20480
	v_mfma_f32_16x16x32_f16 v[78:81], v[110:113], v[98:101], v[78:81]
	v_mfma_f32_16x16x32_f16 v[82:85], v[114:117], v[98:101], v[82:85]
	v_mfma_f32_16x16x32_f16 v[26:29], v[118:121], v[98:101], v[26:29]
	v_mfma_f32_16x16x32_f16 v[50:53], v[110:113], v[102:105], v[50:53]
	v_mfma_f32_16x16x32_f16 v[54:57], v[114:117], v[102:105], v[54:57]
	v_mfma_f32_16x16x32_f16 v[42:45], v[118:121], v[102:105], v[42:45]
	v_mfma_f32_16x16x32_f16 v[58:61], v[110:113], v[106:109], v[58:61]
	v_mfma_f32_16x16x32_f16 v[22:25], v[114:117], v[106:109], v[22:25]
	v_mfma_f32_16x16x32_f16 v[30:33], v[118:121], v[106:109], v[30:33]
	v_add_u32_e32 v21, s19, v122
	s_add_u32 s20, s0, 0x280
	v_readfirstlane_b32 s23, v21
	v_add_u32_e32 v98, 0x2000, v21
	s_waitcnt vmcnt(5) lgkmcnt(0)
	s_barrier
	s_addc_u32 s21, s1, 0
	s_mov_b32 m0, s23
	v_readfirstlane_b32 s19, v98
	global_load_lds_dwordx4 v1, s[20:21]
	s_mov_b32 m0, s19
	v_add_u32_e32 v98, 0x4000, v21
	s_add_u32 s24, s2, 0x280
	global_load_lds_dwordx4 v2, s[20:21]
	v_readfirstlane_b32 s20, v98
	v_add_u32_e32 v98, 0x6000, v21
	s_addc_u32 s25, s3, 0
	s_mov_b32 m0, s20
	v_readfirstlane_b32 s21, v98
	v_add_u32_e32 v21, 0x8000, v21
	global_load_lds_dwordx4 v1, s[24:25]
	s_mov_b32 m0, s21
	v_readfirstlane_b32 s22, v21
	global_load_lds_dwordx4 v2, s[24:25]
	s_mov_b32 m0, s22
	s_nop 0
	global_load_lds_dwordx4 v3, s[24:25]
	s_waitcnt lgkmcnt(0)
	v_mfma_f32_16x16x32_f16 v[34:37], v[74:77], v[90:93], v[34:37]
	v_mfma_f32_16x16x32_f16 v[38:41], v[86:89], v[90:93], v[38:41]
	v_mfma_f32_16x16x32_f16 v[46:49], v[94:97], v[90:93], v[46:49]
	ds_read_b128 v[90:93], v6
	ds_read_b128 v[98:101], v6 offset:2048
	ds_read_b128 v[102:105], v6 offset:4096
	ds_read_b128 v[106:109], v6 offset:6144
	ds_read_b128 v[110:113], v4 offset:16384
	ds_read_b128 v[114:117], v4 offset:18432
	ds_read_b128 v[118:121], v4 offset:20480
	v_mfma_f32_16x16x32_f16 v[78:81], v[74:77], v[62:65], v[78:81]
	v_mfma_f32_16x16x32_f16 v[82:85], v[86:89], v[62:65], v[82:85]
	v_mfma_f32_16x16x32_f16 v[26:29], v[94:97], v[62:65], v[26:29]
	v_mfma_f32_16x16x32_f16 v[50:53], v[74:77], v[66:69], v[50:53]
	v_mfma_f32_16x16x32_f16 v[54:57], v[86:89], v[66:69], v[54:57]
	v_mfma_f32_16x16x32_f16 v[42:45], v[94:97], v[66:69], v[42:45]
	v_mfma_f32_16x16x32_f16 v[58:61], v[74:77], v[70:73], v[58:61]
	v_mfma_f32_16x16x32_f16 v[22:25], v[86:89], v[70:73], v[22:25]
	v_mfma_f32_16x16x32_f16 v[30:33], v[94:97], v[70:73], v[30:33]
	s_waitcnt lgkmcnt(0)
	v_mfma_f32_16x16x32_f16 v[34:37], v[110:113], v[90:93], v[34:37]
	v_mfma_f32_16x16x32_f16 v[38:41], v[114:117], v[90:93], v[38:41]
	v_mfma_f32_16x16x32_f16 v[46:49], v[118:121], v[90:93], v[46:49]
	ds_read_b128 v[62:65], v0
	ds_read_b128 v[66:69], v0 offset:2048
	ds_read_b128 v[70:73], v0 offset:4096
	ds_read_b128 v[74:77], v0 offset:6144
	ds_read_b128 v[86:89], v5 offset:16384
	ds_read_b128 v[90:93], v5 offset:18432
	ds_read_b128 v[94:97], v5 offset:20480
	v_mfma_f32_16x16x32_f16 v[78:81], v[110:113], v[98:101], v[78:81]
	v_mfma_f32_16x16x32_f16 v[82:85], v[114:117], v[98:101], v[82:85]
	v_mfma_f32_16x16x32_f16 v[26:29], v[118:121], v[98:101], v[26:29]
	v_mfma_f32_16x16x32_f16 v[50:53], v[110:113], v[102:105], v[50:53]
	v_mfma_f32_16x16x32_f16 v[54:57], v[114:117], v[102:105], v[54:57]
	v_mfma_f32_16x16x32_f16 v[42:45], v[118:121], v[102:105], v[42:45]
	v_mfma_f32_16x16x32_f16 v[58:61], v[110:113], v[106:109], v[58:61]
	v_mfma_f32_16x16x32_f16 v[22:25], v[114:117], v[106:109], v[22:25]
	v_mfma_f32_16x16x32_f16 v[30:33], v[118:121], v[106:109], v[30:33]
	s_add_u32 s24, s0, 0x300
	s_mov_b32 m0, s13
	s_waitcnt vmcnt(5) lgkmcnt(0)
	s_barrier
	s_addc_u32 s25, s1, 0
	s_add_u32 s26, s2, 0x300
	s_addc_u32 s27, s3, 0
	s_waitcnt lgkmcnt(0)
	v_mfma_f32_16x16x32_f16 v[34:37], v[86:89], v[62:65], v[34:37]
	v_mfma_f32_16x16x32_f16 v[38:41], v[90:93], v[62:65], v[38:41]
	v_mfma_f32_16x16x32_f16 v[46:49], v[94:97], v[62:65], v[46:49]
	ds_read_b128 v[62:65], v6 offset:40960
	ds_read_b128 v[98:101], v6 offset:43008
	ds_read_b128 v[102:105], v6 offset:45056
	ds_read_b128 v[106:109], v6 offset:47104
	ds_read_b128 v[110:113], v4 offset:57344
	ds_read_b128 v[114:117], v4 offset:59392
	ds_read_b128 v[118:121], v4 offset:61440
	v_mfma_f32_16x16x32_f16 v[78:81], v[86:89], v[66:69], v[78:81]
	global_load_lds_dwordx4 v1, s[24:25]
	v_mfma_f32_16x16x32_f16 v[82:85], v[90:93], v[66:69], v[82:85]
	s_mov_b32 m0, s4
	s_nop 0
	global_load_lds_dwordx4 v2, s[24:25]
	v_mfma_f32_16x16x32_f16 v[26:29], v[94:97], v[66:69], v[26:29]
	s_mov_b32 m0, s5
	s_nop 0
	global_load_lds_dwordx4 v1, s[26:27]
	v_mfma_f32_16x16x32_f16 v[50:53], v[86:89], v[70:73], v[50:53]
	s_mov_b32 m0, s6
	s_nop 0
	global_load_lds_dwordx4 v2, s[26:27]
	v_mfma_f32_16x16x32_f16 v[54:57], v[90:93], v[70:73], v[54:57]
	s_mov_b32 m0, s7
	s_nop 0
	global_load_lds_dwordx4 v3, s[26:27]
	v_mfma_f32_16x16x32_f16 v[42:45], v[94:97], v[70:73], v[42:45]
	v_mfma_f32_16x16x32_f16 v[58:61], v[86:89], v[74:77], v[58:61]
	v_mfma_f32_16x16x32_f16 v[22:25], v[90:93], v[74:77], v[22:25]
	v_mfma_f32_16x16x32_f16 v[30:33], v[94:97], v[74:77], v[30:33]
	s_waitcnt lgkmcnt(0)
	v_mfma_f32_16x16x32_f16 v[34:37], v[110:113], v[62:65], v[34:37]
	v_mfma_f32_16x16x32_f16 v[38:41], v[114:117], v[62:65], v[38:41]
	v_mfma_f32_16x16x32_f16 v[46:49], v[118:121], v[62:65], v[46:49]
	ds_read_b128 v[62:65], v0 offset:40960
	ds_read_b128 v[66:69], v0 offset:43008
	ds_read_b128 v[70:73], v0 offset:45056
	ds_read_b128 v[74:77], v0 offset:47104
	ds_read_b128 v[86:89], v5 offset:57344
	ds_read_b128 v[90:93], v5 offset:59392
	ds_read_b128 v[94:97], v5 offset:61440
	v_mfma_f32_16x16x32_f16 v[78:81], v[110:113], v[98:101], v[78:81]
	v_mfma_f32_16x16x32_f16 v[82:85], v[114:117], v[98:101], v[82:85]
	v_mfma_f32_16x16x32_f16 v[26:29], v[118:121], v[98:101], v[26:29]
	v_mfma_f32_16x16x32_f16 v[50:53], v[110:113], v[102:105], v[50:53]
	v_mfma_f32_16x16x32_f16 v[54:57], v[114:117], v[102:105], v[54:57]
	v_mfma_f32_16x16x32_f16 v[42:45], v[118:121], v[102:105], v[42:45]
	v_mfma_f32_16x16x32_f16 v[58:61], v[110:113], v[106:109], v[58:61]
	v_mfma_f32_16x16x32_f16 v[22:25], v[114:117], v[106:109], v[22:25]
	v_mfma_f32_16x16x32_f16 v[30:33], v[118:121], v[106:109], v[30:33]
	s_add_u32 s24, s0, 0x380
	s_mov_b32 m0, s18
	s_waitcnt vmcnt(5) lgkmcnt(0)
	s_barrier
	s_addc_u32 s25, s1, 0
	s_add_u32 s26, s2, 0x380
	s_addc_u32 s27, s3, 0
	s_waitcnt lgkmcnt(0)
	v_mfma_f32_16x16x32_f16 v[34:37], v[86:89], v[62:65], v[34:37]
	v_mfma_f32_16x16x32_f16 v[38:41], v[90:93], v[62:65], v[38:41]
	v_mfma_f32_16x16x32_f16 v[46:49], v[94:97], v[62:65], v[46:49]
	ds_read_b128 v[62:65], v13
	ds_read_b128 v[98:101], v14
	ds_read_b128 v[102:105], v15
	ds_read_b128 v[106:109], v16
	ds_read_b128 v[110:113], v18
	ds_read_b128 v[114:117], v19
	ds_read_b128 v[118:121], v20
	v_mfma_f32_16x16x32_f16 v[78:81], v[86:89], v[66:69], v[78:81]
	global_load_lds_dwordx4 v1, s[24:25]
	v_mfma_f32_16x16x32_f16 v[82:85], v[90:93], v[66:69], v[82:85]
	s_mov_b32 m0, s14
	s_nop 0
	global_load_lds_dwordx4 v2, s[24:25]
	v_mfma_f32_16x16x32_f16 v[26:29], v[94:97], v[66:69], v[26:29]
	s_mov_b32 m0, s15
	s_nop 0
	global_load_lds_dwordx4 v1, s[26:27]
	v_mfma_f32_16x16x32_f16 v[50:53], v[86:89], v[70:73], v[50:53]
	s_mov_b32 m0, s16
	s_nop 0
	global_load_lds_dwordx4 v2, s[26:27]
	v_mfma_f32_16x16x32_f16 v[54:57], v[90:93], v[70:73], v[54:57]
	s_mov_b32 m0, s17
	s_nop 0
	global_load_lds_dwordx4 v3, s[26:27]
	v_mfma_f32_16x16x32_f16 v[42:45], v[94:97], v[70:73], v[42:45]
	v_mfma_f32_16x16x32_f16 v[58:61], v[86:89], v[74:77], v[58:61]
	v_mfma_f32_16x16x32_f16 v[22:25], v[90:93], v[74:77], v[22:25]
	v_mfma_f32_16x16x32_f16 v[30:33], v[94:97], v[74:77], v[30:33]
	s_waitcnt lgkmcnt(0)
	v_mfma_f32_16x16x32_f16 v[34:37], v[110:113], v[62:65], v[34:37]
	v_mfma_f32_16x16x32_f16 v[38:41], v[114:117], v[62:65], v[38:41]
	v_mfma_f32_16x16x32_f16 v[46:49], v[118:121], v[62:65], v[46:49]
	ds_read_b128 v[62:65], v17 offset:2048
	ds_read_b128 v[66:69], v17 offset:4096
	ds_read_b128 v[70:73], v17 offset:6144
	ds_read_b128 v[74:77], v7 offset:16384
	ds_read_b128 v[86:89], v7 offset:18432
	ds_read_b128 v[90:93], v17
	ds_read_b128 v[94:97], v7 offset:20480
	v_mfma_f32_16x16x32_f16 v[78:81], v[110:113], v[98:101], v[78:81]
	v_mfma_f32_16x16x32_f16 v[82:85], v[114:117], v[98:101], v[82:85]
	v_mfma_f32_16x16x32_f16 v[26:29], v[118:121], v[98:101], v[26:29]
	v_mfma_f32_16x16x32_f16 v[50:53], v[110:113], v[102:105], v[50:53]
	v_mfma_f32_16x16x32_f16 v[54:57], v[114:117], v[102:105], v[54:57]
	v_mfma_f32_16x16x32_f16 v[42:45], v[118:121], v[102:105], v[42:45]
	v_mfma_f32_16x16x32_f16 v[58:61], v[110:113], v[106:109], v[58:61]
	v_mfma_f32_16x16x32_f16 v[22:25], v[114:117], v[106:109], v[22:25]
	v_mfma_f32_16x16x32_f16 v[30:33], v[118:121], v[106:109], v[30:33]
	s_add_u32 s24, s0, 0x400
	s_mov_b32 m0, s23
	s_waitcnt vmcnt(5) lgkmcnt(0)
	s_barrier
	s_addc_u32 s25, s1, 0
	s_add_u32 s26, s2, 0x400
	s_addc_u32 s27, s3, 0
	s_waitcnt lgkmcnt(0)
	v_mfma_f32_16x16x32_f16 v[34:37], v[74:77], v[90:93], v[34:37]
	v_mfma_f32_16x16x32_f16 v[38:41], v[86:89], v[90:93], v[38:41]
	v_mfma_f32_16x16x32_f16 v[46:49], v[94:97], v[90:93], v[46:49]
	ds_read_b128 v[90:93], v6
	ds_read_b128 v[98:101], v6 offset:2048
	ds_read_b128 v[102:105], v6 offset:4096
	ds_read_b128 v[106:109], v6 offset:6144
	ds_read_b128 v[110:113], v4 offset:16384
	ds_read_b128 v[114:117], v4 offset:18432
	ds_read_b128 v[118:121], v4 offset:20480
	v_mfma_f32_16x16x32_f16 v[78:81], v[74:77], v[62:65], v[78:81]
	global_load_lds_dwordx4 v1, s[24:25]
	v_mfma_f32_16x16x32_f16 v[82:85], v[86:89], v[62:65], v[82:85]
	s_mov_b32 m0, s19
	s_nop 0
	global_load_lds_dwordx4 v2, s[24:25]
	v_mfma_f32_16x16x32_f16 v[26:29], v[94:97], v[62:65], v[26:29]
	s_mov_b32 m0, s20
	s_nop 0
	global_load_lds_dwordx4 v1, s[26:27]
	v_mfma_f32_16x16x32_f16 v[50:53], v[74:77], v[66:69], v[50:53]
	s_mov_b32 m0, s21
	s_nop 0
	global_load_lds_dwordx4 v2, s[26:27]
	v_mfma_f32_16x16x32_f16 v[54:57], v[86:89], v[66:69], v[54:57]
	s_mov_b32 m0, s22
	s_nop 0
	global_load_lds_dwordx4 v3, s[26:27]
	v_mfma_f32_16x16x32_f16 v[42:45], v[94:97], v[66:69], v[42:45]
	v_mfma_f32_16x16x32_f16 v[58:61], v[74:77], v[70:73], v[58:61]
	v_mfma_f32_16x16x32_f16 v[22:25], v[86:89], v[70:73], v[22:25]
	v_mfma_f32_16x16x32_f16 v[30:33], v[94:97], v[70:73], v[30:33]
	s_waitcnt lgkmcnt(0)
	v_mfma_f32_16x16x32_f16 v[34:37], v[110:113], v[90:93], v[34:37]
	v_mfma_f32_16x16x32_f16 v[38:41], v[114:117], v[90:93], v[38:41]
	v_mfma_f32_16x16x32_f16 v[46:49], v[118:121], v[90:93], v[46:49]
	ds_read_b128 v[62:65], v0
	ds_read_b128 v[66:69], v0 offset:2048
	ds_read_b128 v[70:73], v0 offset:4096
	ds_read_b128 v[74:77], v0 offset:6144
	ds_read_b128 v[86:89], v5 offset:16384
	ds_read_b128 v[90:93], v5 offset:18432
	ds_read_b128 v[94:97], v5 offset:20480
	v_mfma_f32_16x16x32_f16 v[78:81], v[110:113], v[98:101], v[78:81]
	v_mfma_f32_16x16x32_f16 v[82:85], v[114:117], v[98:101], v[82:85]
	v_mfma_f32_16x16x32_f16 v[26:29], v[118:121], v[98:101], v[26:29]
	v_mfma_f32_16x16x32_f16 v[50:53], v[110:113], v[102:105], v[50:53]
	v_mfma_f32_16x16x32_f16 v[54:57], v[114:117], v[102:105], v[54:57]
	v_mfma_f32_16x16x32_f16 v[42:45], v[118:121], v[102:105], v[42:45]
	v_mfma_f32_16x16x32_f16 v[58:61], v[110:113], v[106:109], v[58:61]
	v_mfma_f32_16x16x32_f16 v[22:25], v[114:117], v[106:109], v[22:25]
	v_mfma_f32_16x16x32_f16 v[30:33], v[118:121], v[106:109], v[30:33]
	s_add_u32 s24, s0, 0x480
	s_mov_b32 m0, s13
	s_waitcnt vmcnt(5) lgkmcnt(0)
	s_barrier
	s_addc_u32 s25, s1, 0
	s_add_u32 s26, s2, 0x480
	s_addc_u32 s27, s3, 0
	s_waitcnt lgkmcnt(0)
	v_mfma_f32_16x16x32_f16 v[34:37], v[86:89], v[62:65], v[34:37]
	v_mfma_f32_16x16x32_f16 v[38:41], v[90:93], v[62:65], v[38:41]
	v_mfma_f32_16x16x32_f16 v[46:49], v[94:97], v[62:65], v[46:49]
	ds_read_b128 v[62:65], v6 offset:40960
	ds_read_b128 v[98:101], v6 offset:43008
	ds_read_b128 v[102:105], v6 offset:45056
	ds_read_b128 v[106:109], v6 offset:47104
	ds_read_b128 v[110:113], v4 offset:57344
	ds_read_b128 v[114:117], v4 offset:59392
	ds_read_b128 v[118:121], v4 offset:61440
	v_mfma_f32_16x16x32_f16 v[78:81], v[86:89], v[66:69], v[78:81]
	global_load_lds_dwordx4 v1, s[24:25]
	v_mfma_f32_16x16x32_f16 v[82:85], v[90:93], v[66:69], v[82:85]
	s_mov_b32 m0, s4
	s_nop 0
	global_load_lds_dwordx4 v2, s[24:25]
	v_mfma_f32_16x16x32_f16 v[26:29], v[94:97], v[66:69], v[26:29]
	s_mov_b32 m0, s5
	s_nop 0
	global_load_lds_dwordx4 v1, s[26:27]
	v_mfma_f32_16x16x32_f16 v[50:53], v[86:89], v[70:73], v[50:53]
	s_mov_b32 m0, s6
	s_nop 0
	global_load_lds_dwordx4 v2, s[26:27]
	v_mfma_f32_16x16x32_f16 v[54:57], v[90:93], v[70:73], v[54:57]
	s_mov_b32 m0, s7
	s_nop 0
	global_load_lds_dwordx4 v3, s[26:27]
	v_mfma_f32_16x16x32_f16 v[42:45], v[94:97], v[70:73], v[42:45]
	v_mfma_f32_16x16x32_f16 v[58:61], v[86:89], v[74:77], v[58:61]
	v_mfma_f32_16x16x32_f16 v[22:25], v[90:93], v[74:77], v[22:25]
	v_mfma_f32_16x16x32_f16 v[30:33], v[94:97], v[74:77], v[30:33]
	s_waitcnt lgkmcnt(0)
	v_mfma_f32_16x16x32_f16 v[34:37], v[110:113], v[62:65], v[34:37]
	v_mfma_f32_16x16x32_f16 v[38:41], v[114:117], v[62:65], v[38:41]
	v_mfma_f32_16x16x32_f16 v[46:49], v[118:121], v[62:65], v[46:49]
	ds_read_b128 v[62:65], v0 offset:40960
	ds_read_b128 v[66:69], v0 offset:43008
	ds_read_b128 v[70:73], v0 offset:45056
	ds_read_b128 v[74:77], v0 offset:47104
	ds_read_b128 v[86:89], v5 offset:57344
	ds_read_b128 v[90:93], v5 offset:59392
	ds_read_b128 v[94:97], v5 offset:61440
	v_mfma_f32_16x16x32_f16 v[78:81], v[110:113], v[98:101], v[78:81]
	v_mfma_f32_16x16x32_f16 v[82:85], v[114:117], v[98:101], v[82:85]
	v_mfma_f32_16x16x32_f16 v[26:29], v[118:121], v[98:101], v[26:29]
	v_mfma_f32_16x16x32_f16 v[50:53], v[110:113], v[102:105], v[50:53]
	v_mfma_f32_16x16x32_f16 v[54:57], v[114:117], v[102:105], v[54:57]
	v_mfma_f32_16x16x32_f16 v[42:45], v[118:121], v[102:105], v[42:45]
	v_mfma_f32_16x16x32_f16 v[58:61], v[110:113], v[106:109], v[58:61]
	v_mfma_f32_16x16x32_f16 v[22:25], v[114:117], v[106:109], v[22:25]
	v_mfma_f32_16x16x32_f16 v[30:33], v[118:121], v[106:109], v[30:33]
	s_add_u32 s24, s0, 0x500
	s_mov_b32 m0, s18
	s_waitcnt vmcnt(5) lgkmcnt(0)
	s_barrier
	s_addc_u32 s25, s1, 0
	s_add_u32 s26, s2, 0x500
	s_addc_u32 s27, s3, 0
	s_waitcnt lgkmcnt(0)
	v_mfma_f32_16x16x32_f16 v[34:37], v[86:89], v[62:65], v[34:37]
	v_mfma_f32_16x16x32_f16 v[38:41], v[90:93], v[62:65], v[38:41]
	v_mfma_f32_16x16x32_f16 v[46:49], v[94:97], v[62:65], v[46:49]
	ds_read_b128 v[62:65], v13
	ds_read_b128 v[98:101], v14
	ds_read_b128 v[102:105], v15
	ds_read_b128 v[106:109], v16
	ds_read_b128 v[110:113], v18
	ds_read_b128 v[114:117], v19
	ds_read_b128 v[118:121], v20
	v_mfma_f32_16x16x32_f16 v[78:81], v[86:89], v[66:69], v[78:81]
	global_load_lds_dwordx4 v1, s[24:25]
	v_mfma_f32_16x16x32_f16 v[82:85], v[90:93], v[66:69], v[82:85]
	s_mov_b32 m0, s14
	s_nop 0
	global_load_lds_dwordx4 v2, s[24:25]
	v_mfma_f32_16x16x32_f16 v[26:29], v[94:97], v[66:69], v[26:29]
	s_mov_b32 m0, s15
	s_nop 0
	global_load_lds_dwordx4 v1, s[26:27]
	v_mfma_f32_16x16x32_f16 v[50:53], v[86:89], v[70:73], v[50:53]
	s_mov_b32 m0, s16
	s_nop 0
	global_load_lds_dwordx4 v2, s[26:27]
	v_mfma_f32_16x16x32_f16 v[54:57], v[90:93], v[70:73], v[54:57]
	s_mov_b32 m0, s17
	s_nop 0
	global_load_lds_dwordx4 v3, s[26:27]
	v_mfma_f32_16x16x32_f16 v[42:45], v[94:97], v[70:73], v[42:45]
	v_mfma_f32_16x16x32_f16 v[58:61], v[86:89], v[74:77], v[58:61]
	v_mfma_f32_16x16x32_f16 v[22:25], v[90:93], v[74:77], v[22:25]
	v_mfma_f32_16x16x32_f16 v[30:33], v[94:97], v[74:77], v[30:33]
	s_waitcnt lgkmcnt(0)
	v_mfma_f32_16x16x32_f16 v[34:37], v[110:113], v[62:65], v[34:37]
	v_mfma_f32_16x16x32_f16 v[38:41], v[114:117], v[62:65], v[38:41]
	v_mfma_f32_16x16x32_f16 v[46:49], v[118:121], v[62:65], v[46:49]
	ds_read_b128 v[62:65], v17 offset:2048
	ds_read_b128 v[66:69], v17 offset:4096
	ds_read_b128 v[70:73], v17 offset:6144
	ds_read_b128 v[74:77], v7 offset:16384
	ds_read_b128 v[86:89], v7 offset:18432
	ds_read_b128 v[90:93], v17
	ds_read_b128 v[94:97], v7 offset:20480
	v_mfma_f32_16x16x32_f16 v[78:81], v[110:113], v[98:101], v[78:81]
	v_mfma_f32_16x16x32_f16 v[82:85], v[114:117], v[98:101], v[82:85]
	v_mfma_f32_16x16x32_f16 v[26:29], v[118:121], v[98:101], v[26:29]
	v_mfma_f32_16x16x32_f16 v[50:53], v[110:113], v[102:105], v[50:53]
	v_mfma_f32_16x16x32_f16 v[54:57], v[114:117], v[102:105], v[54:57]
	v_mfma_f32_16x16x32_f16 v[42:45], v[118:121], v[102:105], v[42:45]
	v_mfma_f32_16x16x32_f16 v[58:61], v[110:113], v[106:109], v[58:61]
	v_mfma_f32_16x16x32_f16 v[22:25], v[114:117], v[106:109], v[22:25]
	v_mfma_f32_16x16x32_f16 v[30:33], v[118:121], v[106:109], v[30:33]
	s_add_u32 s24, s0, 0x580
	s_mov_b32 m0, s23
	s_waitcnt vmcnt(5) lgkmcnt(0)
	s_barrier
	s_addc_u32 s25, s1, 0
	s_add_u32 s26, s2, 0x580
	s_addc_u32 s27, s3, 0
	s_waitcnt lgkmcnt(0)
	v_mfma_f32_16x16x32_f16 v[34:37], v[74:77], v[90:93], v[34:37]
	v_mfma_f32_16x16x32_f16 v[38:41], v[86:89], v[90:93], v[38:41]
	v_mfma_f32_16x16x32_f16 v[46:49], v[94:97], v[90:93], v[46:49]
	ds_read_b128 v[90:93], v6
	ds_read_b128 v[98:101], v6 offset:2048
	ds_read_b128 v[102:105], v6 offset:4096
	ds_read_b128 v[106:109], v6 offset:6144
	ds_read_b128 v[110:113], v4 offset:16384
	ds_read_b128 v[114:117], v4 offset:18432
	ds_read_b128 v[118:121], v4 offset:20480
	v_mfma_f32_16x16x32_f16 v[78:81], v[74:77], v[62:65], v[78:81]
	global_load_lds_dwordx4 v1, s[24:25]
	v_mfma_f32_16x16x32_f16 v[82:85], v[86:89], v[62:65], v[82:85]
	s_mov_b32 m0, s19
	s_nop 0
	global_load_lds_dwordx4 v2, s[24:25]
	v_mfma_f32_16x16x32_f16 v[26:29], v[94:97], v[62:65], v[26:29]
	s_mov_b32 m0, s20
	s_nop 0
	global_load_lds_dwordx4 v1, s[26:27]
	v_mfma_f32_16x16x32_f16 v[50:53], v[74:77], v[66:69], v[50:53]
	s_mov_b32 m0, s21
	s_nop 0
	global_load_lds_dwordx4 v2, s[26:27]
	v_mfma_f32_16x16x32_f16 v[54:57], v[86:89], v[66:69], v[54:57]
	s_mov_b32 m0, s22
	s_nop 0
	global_load_lds_dwordx4 v3, s[26:27]
	v_mfma_f32_16x16x32_f16 v[42:45], v[94:97], v[66:69], v[42:45]
	v_mfma_f32_16x16x32_f16 v[58:61], v[74:77], v[70:73], v[58:61]
	v_mfma_f32_16x16x32_f16 v[22:25], v[86:89], v[70:73], v[22:25]
	v_mfma_f32_16x16x32_f16 v[30:33], v[94:97], v[70:73], v[30:33]
	s_waitcnt lgkmcnt(0)
	v_mfma_f32_16x16x32_f16 v[34:37], v[110:113], v[90:93], v[34:37]
	v_mfma_f32_16x16x32_f16 v[38:41], v[114:117], v[90:93], v[38:41]
	v_mfma_f32_16x16x32_f16 v[46:49], v[118:121], v[90:93], v[46:49]
	ds_read_b128 v[62:65], v0
	ds_read_b128 v[66:69], v0 offset:2048
	ds_read_b128 v[70:73], v0 offset:4096
	ds_read_b128 v[74:77], v0 offset:6144
	ds_read_b128 v[86:89], v5 offset:16384
	ds_read_b128 v[90:93], v5 offset:18432
	ds_read_b128 v[94:97], v5 offset:20480
	v_mfma_f32_16x16x32_f16 v[78:81], v[110:113], v[98:101], v[78:81]
	v_mfma_f32_16x16x32_f16 v[82:85], v[114:117], v[98:101], v[82:85]
	v_mfma_f32_16x16x32_f16 v[26:29], v[118:121], v[98:101], v[26:29]
	v_mfma_f32_16x16x32_f16 v[50:53], v[110:113], v[102:105], v[50:53]
	v_mfma_f32_16x16x32_f16 v[54:57], v[114:117], v[102:105], v[54:57]
	v_mfma_f32_16x16x32_f16 v[42:45], v[118:121], v[102:105], v[42:45]
	v_mfma_f32_16x16x32_f16 v[58:61], v[110:113], v[106:109], v[58:61]
	v_mfma_f32_16x16x32_f16 v[22:25], v[114:117], v[106:109], v[22:25]
	v_mfma_f32_16x16x32_f16 v[30:33], v[118:121], v[106:109], v[30:33]
	s_add_u32 s24, s0, 0x600
	s_mov_b32 m0, s13
	s_waitcnt vmcnt(5) lgkmcnt(0)
	s_barrier
	s_addc_u32 s25, s1, 0
	s_add_u32 s26, s2, 0x600
	s_addc_u32 s27, s3, 0
	s_waitcnt lgkmcnt(0)
	v_mfma_f32_16x16x32_f16 v[34:37], v[86:89], v[62:65], v[34:37]
	v_mfma_f32_16x16x32_f16 v[38:41], v[90:93], v[62:65], v[38:41]
	v_mfma_f32_16x16x32_f16 v[46:49], v[94:97], v[62:65], v[46:49]
	ds_read_b128 v[62:65], v6 offset:40960
	ds_read_b128 v[98:101], v6 offset:43008
	ds_read_b128 v[102:105], v6 offset:45056
	ds_read_b128 v[106:109], v6 offset:47104
	ds_read_b128 v[110:113], v4 offset:57344
	ds_read_b128 v[114:117], v4 offset:59392
	ds_read_b128 v[118:121], v4 offset:61440
	v_mfma_f32_16x16x32_f16 v[78:81], v[86:89], v[66:69], v[78:81]
	global_load_lds_dwordx4 v1, s[24:25]
	v_mfma_f32_16x16x32_f16 v[82:85], v[90:93], v[66:69], v[82:85]
	s_mov_b32 m0, s4
	s_nop 0
	global_load_lds_dwordx4 v2, s[24:25]
	v_mfma_f32_16x16x32_f16 v[26:29], v[94:97], v[66:69], v[26:29]
	s_mov_b32 m0, s5
	s_nop 0
	global_load_lds_dwordx4 v1, s[26:27]
	v_mfma_f32_16x16x32_f16 v[50:53], v[86:89], v[70:73], v[50:53]
	s_mov_b32 m0, s6
	s_nop 0
	global_load_lds_dwordx4 v2, s[26:27]
	v_mfma_f32_16x16x32_f16 v[54:57], v[90:93], v[70:73], v[54:57]
	s_mov_b32 m0, s7
	s_nop 0
	global_load_lds_dwordx4 v3, s[26:27]
	v_mfma_f32_16x16x32_f16 v[42:45], v[94:97], v[70:73], v[42:45]
	v_mfma_f32_16x16x32_f16 v[58:61], v[86:89], v[74:77], v[58:61]
	v_mfma_f32_16x16x32_f16 v[22:25], v[90:93], v[74:77], v[22:25]
	v_mfma_f32_16x16x32_f16 v[30:33], v[94:97], v[74:77], v[30:33]
	s_waitcnt lgkmcnt(0)
	v_mfma_f32_16x16x32_f16 v[34:37], v[110:113], v[62:65], v[34:37]
	v_mfma_f32_16x16x32_f16 v[38:41], v[114:117], v[62:65], v[38:41]
	v_mfma_f32_16x16x32_f16 v[46:49], v[118:121], v[62:65], v[46:49]
	ds_read_b128 v[62:65], v0 offset:40960
	ds_read_b128 v[66:69], v0 offset:43008
	ds_read_b128 v[70:73], v0 offset:45056
	ds_read_b128 v[74:77], v0 offset:47104
	ds_read_b128 v[86:89], v5 offset:57344
	ds_read_b128 v[90:93], v5 offset:59392
	ds_read_b128 v[94:97], v5 offset:61440
	v_mfma_f32_16x16x32_f16 v[78:81], v[110:113], v[98:101], v[78:81]
	v_mfma_f32_16x16x32_f16 v[82:85], v[114:117], v[98:101], v[82:85]
	v_mfma_f32_16x16x32_f16 v[26:29], v[118:121], v[98:101], v[26:29]
	v_mfma_f32_16x16x32_f16 v[50:53], v[110:113], v[102:105], v[50:53]
	v_mfma_f32_16x16x32_f16 v[54:57], v[114:117], v[102:105], v[54:57]
	v_mfma_f32_16x16x32_f16 v[42:45], v[118:121], v[102:105], v[42:45]
	v_mfma_f32_16x16x32_f16 v[58:61], v[110:113], v[106:109], v[58:61]
	v_mfma_f32_16x16x32_f16 v[22:25], v[114:117], v[106:109], v[22:25]
	v_mfma_f32_16x16x32_f16 v[30:33], v[118:121], v[106:109], v[30:33]
	s_add_u32 s24, s0, 0x680
	s_mov_b32 m0, s18
	s_waitcnt vmcnt(5) lgkmcnt(0)
	s_barrier
	s_addc_u32 s25, s1, 0
	s_add_u32 s26, s2, 0x680
	s_addc_u32 s27, s3, 0
	s_waitcnt lgkmcnt(0)
	v_mfma_f32_16x16x32_f16 v[34:37], v[86:89], v[62:65], v[34:37]
	v_mfma_f32_16x16x32_f16 v[38:41], v[90:93], v[62:65], v[38:41]
	v_mfma_f32_16x16x32_f16 v[46:49], v[94:97], v[62:65], v[46:49]
	ds_read_b128 v[62:65], v13
	ds_read_b128 v[98:101], v14
	ds_read_b128 v[102:105], v15
	ds_read_b128 v[106:109], v16
	ds_read_b128 v[110:113], v18
	ds_read_b128 v[114:117], v19
	ds_read_b128 v[118:121], v20
	v_mfma_f32_16x16x32_f16 v[78:81], v[86:89], v[66:69], v[78:81]
	global_load_lds_dwordx4 v1, s[24:25]
	v_mfma_f32_16x16x32_f16 v[82:85], v[90:93], v[66:69], v[82:85]
	s_mov_b32 m0, s14
	s_nop 0
	global_load_lds_dwordx4 v2, s[24:25]
	v_mfma_f32_16x16x32_f16 v[26:29], v[94:97], v[66:69], v[26:29]
	s_mov_b32 m0, s15
	s_nop 0
	global_load_lds_dwordx4 v1, s[26:27]
	v_mfma_f32_16x16x32_f16 v[50:53], v[86:89], v[70:73], v[50:53]
	s_mov_b32 m0, s16
	s_nop 0
	global_load_lds_dwordx4 v2, s[26:27]
	v_mfma_f32_16x16x32_f16 v[54:57], v[90:93], v[70:73], v[54:57]
	s_mov_b32 m0, s17
	s_nop 0
	global_load_lds_dwordx4 v3, s[26:27]
	v_mfma_f32_16x16x32_f16 v[42:45], v[94:97], v[70:73], v[42:45]
	v_mfma_f32_16x16x32_f16 v[58:61], v[86:89], v[74:77], v[58:61]
	v_mfma_f32_16x16x32_f16 v[22:25], v[90:93], v[74:77], v[22:25]
	v_mfma_f32_16x16x32_f16 v[30:33], v[94:97], v[74:77], v[30:33]
	s_waitcnt lgkmcnt(0)
	v_mfma_f32_16x16x32_f16 v[34:37], v[110:113], v[62:65], v[34:37]
	v_mfma_f32_16x16x32_f16 v[38:41], v[114:117], v[62:65], v[38:41]
	v_mfma_f32_16x16x32_f16 v[46:49], v[118:121], v[62:65], v[46:49]
	ds_read_b128 v[62:65], v17 offset:2048
	ds_read_b128 v[66:69], v17 offset:4096
	ds_read_b128 v[70:73], v17 offset:6144
	ds_read_b128 v[74:77], v7 offset:16384
	ds_read_b128 v[86:89], v7 offset:18432
	ds_read_b128 v[90:93], v17
	ds_read_b128 v[94:97], v7 offset:20480
	v_mfma_f32_16x16x32_f16 v[78:81], v[110:113], v[98:101], v[78:81]
	v_mfma_f32_16x16x32_f16 v[82:85], v[114:117], v[98:101], v[82:85]
	v_mfma_f32_16x16x32_f16 v[26:29], v[118:121], v[98:101], v[26:29]
	v_mfma_f32_16x16x32_f16 v[50:53], v[110:113], v[102:105], v[50:53]
	v_mfma_f32_16x16x32_f16 v[54:57], v[114:117], v[102:105], v[54:57]
	v_mfma_f32_16x16x32_f16 v[42:45], v[118:121], v[102:105], v[42:45]
	v_mfma_f32_16x16x32_f16 v[58:61], v[110:113], v[106:109], v[58:61]
	v_mfma_f32_16x16x32_f16 v[22:25], v[114:117], v[106:109], v[22:25]
	v_mfma_f32_16x16x32_f16 v[30:33], v[118:121], v[106:109], v[30:33]
	s_add_u32 s14, s0, 0x700
	s_mov_b32 m0, s23
	s_waitcnt vmcnt(5) lgkmcnt(0)
	s_barrier
	s_addc_u32 s15, s1, 0
	s_add_u32 s16, s2, 0x700
	s_addc_u32 s17, s3, 0
	s_waitcnt lgkmcnt(0)
	v_mfma_f32_16x16x32_f16 v[34:37], v[74:77], v[90:93], v[34:37]
	v_mfma_f32_16x16x32_f16 v[38:41], v[86:89], v[90:93], v[38:41]
	v_mfma_f32_16x16x32_f16 v[46:49], v[94:97], v[90:93], v[46:49]
	ds_read_b128 v[90:93], v6
	ds_read_b128 v[98:101], v6 offset:2048
	ds_read_b128 v[102:105], v6 offset:4096
	ds_read_b128 v[106:109], v6 offset:6144
	ds_read_b128 v[110:113], v4 offset:16384
	ds_read_b128 v[114:117], v4 offset:18432
	ds_read_b128 v[118:121], v4 offset:20480
	v_mfma_f32_16x16x32_f16 v[78:81], v[74:77], v[62:65], v[78:81]
	global_load_lds_dwordx4 v1, s[14:15]
	v_mfma_f32_16x16x32_f16 v[82:85], v[86:89], v[62:65], v[82:85]
	s_mov_b32 m0, s19
	s_nop 0
	global_load_lds_dwordx4 v2, s[14:15]
	v_mfma_f32_16x16x32_f16 v[26:29], v[94:97], v[62:65], v[26:29]
	s_mov_b32 m0, s20
	s_nop 0
	global_load_lds_dwordx4 v1, s[16:17]
	v_mfma_f32_16x16x32_f16 v[50:53], v[74:77], v[66:69], v[50:53]
	s_mov_b32 m0, s21
	s_nop 0
	global_load_lds_dwordx4 v2, s[16:17]
	v_mfma_f32_16x16x32_f16 v[54:57], v[86:89], v[66:69], v[54:57]
	s_mov_b32 m0, s22
	s_nop 0
	global_load_lds_dwordx4 v3, s[16:17]
	v_mfma_f32_16x16x32_f16 v[42:45], v[94:97], v[66:69], v[42:45]
	v_mfma_f32_16x16x32_f16 v[58:61], v[74:77], v[70:73], v[58:61]
	v_mfma_f32_16x16x32_f16 v[22:25], v[86:89], v[70:73], v[22:25]
	v_mfma_f32_16x16x32_f16 v[30:33], v[94:97], v[70:73], v[30:33]
	s_waitcnt lgkmcnt(0)
	v_mfma_f32_16x16x32_f16 v[34:37], v[110:113], v[90:93], v[34:37]
	v_mfma_f32_16x16x32_f16 v[38:41], v[114:117], v[90:93], v[38:41]
	v_mfma_f32_16x16x32_f16 v[46:49], v[118:121], v[90:93], v[46:49]
	ds_read_b128 v[62:65], v0
	ds_read_b128 v[66:69], v0 offset:2048
	ds_read_b128 v[70:73], v0 offset:4096
	ds_read_b128 v[74:77], v0 offset:6144
	ds_read_b128 v[86:89], v5 offset:16384
	ds_read_b128 v[90:93], v5 offset:18432
	ds_read_b128 v[94:97], v5 offset:20480
	v_mfma_f32_16x16x32_f16 v[78:81], v[110:113], v[98:101], v[78:81]
	v_mfma_f32_16x16x32_f16 v[82:85], v[114:117], v[98:101], v[82:85]
	v_mfma_f32_16x16x32_f16 v[26:29], v[118:121], v[98:101], v[26:29]
	v_mfma_f32_16x16x32_f16 v[50:53], v[110:113], v[102:105], v[50:53]
	v_mfma_f32_16x16x32_f16 v[54:57], v[114:117], v[102:105], v[54:57]
	v_mfma_f32_16x16x32_f16 v[42:45], v[118:121], v[102:105], v[42:45]
	v_mfma_f32_16x16x32_f16 v[58:61], v[110:113], v[106:109], v[58:61]
	v_mfma_f32_16x16x32_f16 v[22:25], v[114:117], v[106:109], v[22:25]
	v_mfma_f32_16x16x32_f16 v[30:33], v[118:121], v[106:109], v[30:33]
	s_add_u32 s0, s0, 0x780
	s_mov_b32 m0, s13
	s_waitcnt vmcnt(5) lgkmcnt(0)
	s_barrier
	s_addc_u32 s1, s1, 0
	s_add_u32 s2, s2, 0x780
	s_addc_u32 s3, s3, 0
	s_waitcnt lgkmcnt(0)
	v_mfma_f32_16x16x32_f16 v[34:37], v[86:89], v[62:65], v[34:37]
	v_mfma_f32_16x16x32_f16 v[38:41], v[90:93], v[62:65], v[38:41]
	v_mfma_f32_16x16x32_f16 v[46:49], v[94:97], v[62:65], v[46:49]
	ds_read_b128 v[62:65], v6 offset:40960
	ds_read_b128 v[98:101], v6 offset:43008
	ds_read_b128 v[102:105], v6 offset:45056
	ds_read_b128 v[106:109], v6 offset:47104
	ds_read_b128 v[110:113], v4 offset:57344
	ds_read_b128 v[114:117], v4 offset:59392
	ds_read_b128 v[118:121], v4 offset:61440
	v_mfma_f32_16x16x32_f16 v[78:81], v[86:89], v[66:69], v[78:81]
	global_load_lds_dwordx4 v1, s[0:1]
	v_mfma_f32_16x16x32_f16 v[82:85], v[90:93], v[66:69], v[82:85]
	s_mov_b32 m0, s4
	s_nop 0
	global_load_lds_dwordx4 v2, s[0:1]
	v_mfma_f32_16x16x32_f16 v[26:29], v[94:97], v[66:69], v[26:29]
	s_mov_b32 m0, s5
	s_nop 0
	global_load_lds_dwordx4 v1, s[2:3]
	v_mfma_f32_16x16x32_f16 v[50:53], v[86:89], v[70:73], v[50:53]
	s_mov_b32 m0, s6
	s_nop 0
	global_load_lds_dwordx4 v2, s[2:3]
	v_mfma_f32_16x16x32_f16 v[54:57], v[90:93], v[70:73], v[54:57]
	s_mov_b32 m0, s7
	s_nop 0
	global_load_lds_dwordx4 v3, s[2:3]
	v_mfma_f32_16x16x32_f16 v[42:45], v[94:97], v[70:73], v[42:45]
	v_mfma_f32_16x16x32_f16 v[58:61], v[86:89], v[74:77], v[58:61]
	v_mfma_f32_16x16x32_f16 v[22:25], v[90:93], v[74:77], v[22:25]
	v_mfma_f32_16x16x32_f16 v[30:33], v[94:97], v[74:77], v[30:33]
	s_waitcnt lgkmcnt(0)
	v_mfma_f32_16x16x32_f16 v[34:37], v[110:113], v[62:65], v[34:37]
	v_mfma_f32_16x16x32_f16 v[38:41], v[114:117], v[62:65], v[38:41]
	v_mfma_f32_16x16x32_f16 v[46:49], v[118:121], v[62:65], v[46:49]
	ds_read_b128 v[62:65], v0 offset:40960
	ds_read_b128 v[66:69], v0 offset:43008
	ds_read_b128 v[70:73], v0 offset:45056
	ds_read_b128 v[74:77], v0 offset:47104
	ds_read_b128 v[86:89], v5 offset:57344
	ds_read_b128 v[90:93], v5 offset:59392
	ds_read_b128 v[94:97], v5 offset:61440
	v_mfma_f32_16x16x32_f16 v[78:81], v[110:113], v[98:101], v[78:81]
	v_mfma_f32_16x16x32_f16 v[82:85], v[114:117], v[98:101], v[82:85]
	v_mfma_f32_16x16x32_f16 v[26:29], v[118:121], v[98:101], v[26:29]
	v_mfma_f32_16x16x32_f16 v[50:53], v[110:113], v[102:105], v[50:53]
	v_mfma_f32_16x16x32_f16 v[54:57], v[114:117], v[102:105], v[54:57]
	v_mfma_f32_16x16x32_f16 v[42:45], v[118:121], v[102:105], v[42:45]
	v_mfma_f32_16x16x32_f16 v[58:61], v[110:113], v[106:109], v[58:61]
	v_mfma_f32_16x16x32_f16 v[22:25], v[114:117], v[106:109], v[22:25]
	v_mfma_f32_16x16x32_f16 v[30:33], v[118:121], v[106:109], v[30:33]
	s_waitcnt vmcnt(5) lgkmcnt(0)
	s_barrier
	s_waitcnt lgkmcnt(0)
	v_mfma_f32_16x16x32_f16 v[34:37], v[86:89], v[62:65], v[34:37]
	v_mfma_f32_16x16x32_f16 v[38:41], v[90:93], v[62:65], v[38:41]
	v_mfma_f32_16x16x32_f16 v[46:49], v[94:97], v[62:65], v[46:49]
	ds_read_b128 v[62:65], v13
	ds_read_b128 v[98:101], v14
	ds_read_b128 v[102:105], v15
	ds_read_b128 v[106:109], v16
	ds_read_b128 v[110:113], v18
	ds_read_b128 v[114:117], v19
	ds_read_b128 v[18:21], v20
	v_mfma_f32_16x16x32_f16 v[78:81], v[86:89], v[66:69], v[78:81]
	v_mfma_f32_16x16x32_f16 v[82:85], v[90:93], v[66:69], v[82:85]
	v_mfma_f32_16x16x32_f16 v[26:29], v[94:97], v[66:69], v[26:29]
	v_mfma_f32_16x16x32_f16 v[50:53], v[86:89], v[70:73], v[50:53]
	v_mfma_f32_16x16x32_f16 v[54:57], v[90:93], v[70:73], v[54:57]
	v_mfma_f32_16x16x32_f16 v[42:45], v[94:97], v[70:73], v[42:45]
	v_mfma_f32_16x16x32_f16 v[58:61], v[86:89], v[74:77], v[58:61]
	v_mfma_f32_16x16x32_f16 v[22:25], v[90:93], v[74:77], v[22:25]
	v_mfma_f32_16x16x32_f16 v[30:33], v[94:97], v[74:77], v[30:33]
	s_waitcnt lgkmcnt(0)
	v_mfma_f32_16x16x32_f16 v[34:37], v[110:113], v[62:65], v[34:37]
	v_mfma_f32_16x16x32_f16 v[38:41], v[114:117], v[62:65], v[38:41]
	v_mfma_f32_16x16x32_f16 v[46:49], v[18:21], v[62:65], v[46:49]
	ds_read_b128 v[62:65], v17 offset:2048
	ds_read_b128 v[66:69], v17 offset:4096
	ds_read_b128 v[70:73], v17 offset:6144
	ds_read_b128 v[74:77], v7 offset:16384
	ds_read_b128 v[86:89], v7 offset:18432
	ds_read_b128 v[14:17], v17
	ds_read_b128 v[90:93], v7 offset:20480
	v_mfma_f32_16x16x32_f16 v[78:81], v[110:113], v[98:101], v[78:81]
	v_mfma_f32_16x16x32_f16 v[82:85], v[114:117], v[98:101], v[82:85]
	v_mfma_f32_16x16x32_f16 v[26:29], v[18:21], v[98:101], v[26:29]
	v_mfma_f32_16x16x32_f16 v[50:53], v[110:113], v[102:105], v[50:53]
	v_mfma_f32_16x16x32_f16 v[54:57], v[114:117], v[102:105], v[54:57]
	v_mfma_f32_16x16x32_f16 v[42:45], v[18:21], v[102:105], v[42:45]
	v_mfma_f32_16x16x32_f16 v[58:61], v[110:113], v[106:109], v[58:61]
	v_mfma_f32_16x16x32_f16 v[22:25], v[114:117], v[106:109], v[22:25]
	v_mfma_f32_16x16x32_f16 v[18:21], v[18:21], v[106:109], v[30:33]
	s_waitcnt vmcnt(0) lgkmcnt(0)
	s_barrier
	s_waitcnt lgkmcnt(0)
	v_mfma_f32_16x16x32_f16 v[30:33], v[74:77], v[14:17], v[34:37]
	v_mfma_f32_16x16x32_f16 v[34:37], v[86:89], v[14:17], v[38:41]
	v_mfma_f32_16x16x32_f16 v[14:17], v[90:93], v[14:17], v[46:49]
	s_nop 1
	ds_read_b128 v[38:41], v6
	ds_read_b128 v[46:49], v6 offset:2048
	ds_read_b128 v[94:97], v6 offset:4096
	ds_read_b128 v[98:101], v6 offset:6144
	ds_read_b128 v[102:105], v4 offset:16384
	ds_read_b128 v[106:109], v4 offset:18432
	ds_read_b128 v[110:113], v4 offset:20480
	v_mfma_f32_16x16x32_f16 v[78:81], v[74:77], v[62:65], v[78:81]
	v_mfma_f32_16x16x32_f16 v[82:85], v[86:89], v[62:65], v[82:85]
	v_mfma_f32_16x16x32_f16 v[26:29], v[90:93], v[62:65], v[26:29]
	v_mfma_f32_16x16x32_f16 v[50:53], v[74:77], v[66:69], v[50:53]
	v_mfma_f32_16x16x32_f16 v[54:57], v[86:89], v[66:69], v[54:57]
	v_mfma_f32_16x16x32_f16 v[42:45], v[90:93], v[66:69], v[42:45]
	v_mfma_f32_16x16x32_f16 v[58:61], v[74:77], v[70:73], v[58:61]
	v_mfma_f32_16x16x32_f16 v[22:25], v[86:89], v[70:73], v[22:25]
	v_mfma_f32_16x16x32_f16 v[18:21], v[90:93], v[70:73], v[18:21]
	s_waitcnt lgkmcnt(0)
	v_mfma_f32_16x16x32_f16 v[30:33], v[102:105], v[38:41], v[30:33]
	v_mfma_f32_16x16x32_f16 v[34:37], v[106:109], v[38:41], v[34:37]
	v_mfma_f32_16x16x32_f16 v[14:17], v[110:113], v[38:41], v[14:17]
	ds_read_b128 v[38:41], v0
	ds_read_b128 v[62:65], v0 offset:2048
	ds_read_b128 v[66:69], v0 offset:4096
	ds_read_b128 v[0:3], v0 offset:6144
	ds_read_b128 v[70:73], v5 offset:16384
	ds_read_b128 v[74:77], v5 offset:18432
	ds_read_b128 v[86:89], v5 offset:20480
	v_mfma_f32_16x16x32_f16 v[4:7], v[102:105], v[46:49], v[78:81]
	v_mfma_f32_16x16x32_f16 v[78:81], v[106:109], v[46:49], v[82:85]
	v_mfma_f32_16x16x32_f16 v[26:29], v[110:113], v[46:49], v[26:29]
	v_mfma_f32_16x16x32_f16 v[46:49], v[102:105], v[94:97], v[50:53]
	v_mfma_f32_16x16x32_f16 v[50:53], v[106:109], v[94:97], v[54:57]
	v_mfma_f32_16x16x32_f16 v[42:45], v[110:113], v[94:97], v[42:45]
	v_mfma_f32_16x16x32_f16 v[54:57], v[102:105], v[98:101], v[58:61]
	v_mfma_f32_16x16x32_f16 v[22:25], v[106:109], v[98:101], v[22:25]
	v_mfma_f32_16x16x32_f16 v[18:21], v[110:113], v[98:101], v[18:21]
	s_waitcnt lgkmcnt(0)
	v_mfma_f32_16x16x32_f16 v[30:33], v[70:73], v[38:41], v[30:33]
	v_mfma_f32_16x16x32_f16 v[34:37], v[74:77], v[38:41], v[34:37]
	v_mfma_f32_16x16x32_f16 v[14:17], v[86:89], v[38:41], v[14:17]
	v_mfma_f32_16x16x32_f16 v[38:41], v[70:73], v[62:65], v[4:7]
	v_mfma_f32_16x16x32_f16 v[58:61], v[74:77], v[62:65], v[78:81]
	v_mfma_f32_16x16x32_f16 v[26:29], v[86:89], v[62:65], v[26:29]
	v_mfma_f32_16x16x32_f16 v[46:49], v[70:73], v[66:69], v[46:49]
	v_mfma_f32_16x16x32_f16 v[50:53], v[74:77], v[66:69], v[50:53]
	v_mfma_f32_16x16x32_f16 v[42:45], v[86:89], v[66:69], v[42:45]
	v_mfma_f32_16x16x32_f16 v[54:57], v[70:73], v[0:3], v[54:57]
	v_mfma_f32_16x16x32_f16 v[4:7], v[74:77], v[0:3], v[22:25]
	v_mfma_f32_16x16x32_f16 v[0:3], v[86:89], v[0:3], v[18:21]
	s_lshl_b32 s0, s12, 1
	v_or_b32_e32 v11, s10, v11
	s_and_b32 s5, s0, 0x3fffff0
	s_movk_i32 s0, 0x3c0
	v_mad_u32_u24 v62, v9, 48, s11
	v_lshlrev_b32_e32 v24, 2, v12
	v_and_or_b32 v63, v11, s0, v8
	s_movk_i32 s0, 0x400
	s_mov_b32 s4, 0x3e38aa3b
	v_and_or_b32 v20, v10, 48, v24
	v_pk_mul_f32 v[10:11], v[32:33], s[4:5] op_sel_hi:[1,0]
	v_cmp_gt_u32_e32 vcc, s0, v62
	v_pk_mul_f32 v[12:13], v[30:31], s[4:5] op_sel_hi:[1,0]
	v_lshrrev_b32_e32 v8, 10, v62
	v_cndmask_b32_e32 v9, v33, v11, vcc
	v_cndmask_b32_e32 v11, v32, v10, vcc
	v_lshrrev_b32_e32 v18, 6, v62
	v_cndmask_b32_e32 v10, v31, v13, vcc
	v_cndmask_b32_e32 v12, v30, v12, vcc
	v_cvt_pk_f16_f32 v11, v11, v9
	v_mov_b32_e32 v9, 0
	v_cvt_pk_f16_f32 v10, v12, v10
	v_lshlrev_b64 v[12:13], 22, v[8:9]
	v_and_or_b32 v8, v18, 15, s5
	v_lshlrev_b32_e32 v30, 10, v8
	v_or_b32_e32 v8, v30, v63
	v_lshl_add_u64 v[12:13], s[8:9], 0, v[12:13]
	v_lshlrev_b64 v[18:19], 7, v[8:9]
	v_lshl_add_u64 v[18:19], v[12:13], 0, v[18:19]
	v_lshlrev_b32_e32 v8, 1, v20
	v_lshl_add_u64 v[18:19], v[18:19], 0, v[8:9]
	s_movk_i32 s0, 0x3f0
	global_store_dwordx2 v[18:19], v[10:11], off
	v_add_u32_e32 v11, 16, v62
	v_pk_mul_f32 v[18:19], v[36:37], s[4:5] op_sel_hi:[1,0]
	v_pk_mul_f32 v[20:21], v[34:35], s[4:5] op_sel_hi:[1,0]
	v_cmp_gt_u32_e64 s[0:1], s0, v62
	v_lshrrev_b32_e32 v10, 10, v11
	v_and_or_b32 v23, v11, 48, v24
	v_cndmask_b32_e64 v22, v36, v18, s[0:1]
	v_cndmask_b32_e64 v18, v35, v21, s[0:1]
	v_cndmask_b32_e64 v20, v34, v20, s[0:1]
	v_lshrrev_b32_e32 v21, 6, v11
	v_cvt_pk_f16_f32 v18, v20, v18
	v_and_or_b32 v20, v21, 15, s5
	v_mov_b32_e32 v11, v9
	v_lshlrev_b32_e32 v31, 10, v20
	v_lshlrev_b64 v[10:11], 22, v[10:11]
	v_or_b32_e32 v20, v31, v63
	v_mov_b32_e32 v21, v9
	v_cndmask_b32_e64 v19, v37, v19, s[0:1]
	v_lshl_add_u64 v[10:11], s[8:9], 0, v[10:11]
	v_lshlrev_b64 v[20:21], 7, v[20:21]
	v_cvt_pk_f16_f32 v19, v22, v19
	v_lshl_add_u64 v[20:21], v[10:11], 0, v[20:21]
	v_lshlrev_b32_e32 v22, 1, v23
	v_mov_b32_e32 v23, v9
	v_lshl_add_u64 v[20:21], v[20:21], 0, v[22:23]
	global_store_dwordx2 v[20:21], v[18:19], off
	v_add_u32_e32 v19, 32, v62
	s_movk_i32 s2, 0x3e0
	v_and_or_b32 v33, v19, 48, v24
	v_pk_mul_f32 v[20:21], v[16:17], s[4:5] op_sel_hi:[1,0]
	v_pk_mul_f32 v[24:25], v[14:15], s[4:5] op_sel_hi:[1,0]
	v_cmp_gt_u32_e64 s[2:3], s2, v62
	v_lshrrev_b32_e32 v18, 10, v19
	v_lshrrev_b32_e32 v32, 6, v19
	v_cndmask_b32_e64 v17, v17, v21, s[2:3]
	v_cndmask_b32_e64 v16, v16, v20, s[2:3]
	v_cndmask_b32_e64 v15, v15, v25, s[2:3]
	v_cndmask_b32_e64 v14, v14, v24, s[2:3]
	v_mov_b32_e32 v19, v9
	v_cvt_pk_f16_f32 v14, v14, v15
	v_cvt_pk_f16_f32 v15, v16, v17
	v_lshlrev_b64 v[16:17], 22, v[18:19]
	v_and_or_b32 v18, v32, 15, s5
	v_lshlrev_b32_e32 v24, 10, v18
	v_or_b32_e32 v18, v24, v63
	v_lshl_add_u64 v[16:17], s[8:9], 0, v[16:17]
	v_lshlrev_b64 v[18:19], 7, v[18:19]
	v_lshl_add_u64 v[18:19], v[16:17], 0, v[18:19]
	v_lshlrev_b32_e32 v20, 1, v33
	v_mov_b32_e32 v21, v9
	v_lshl_add_u64 v[18:19], v[18:19], 0, v[20:21]
	global_store_dwordx2 v[18:19], v[14:15], off
	v_pk_mul_f32 v[14:15], v[40:41], s[4:5] op_sel_hi:[1,0]
	v_pk_mul_f32 v[18:19], v[38:39], s[4:5] op_sel_hi:[1,0]
	v_or_b32_e32 v25, 16, v63
	v_cndmask_b32_e32 v32, v40, v14, vcc
	v_cndmask_b32_e32 v14, v39, v19, vcc
	v_cndmask_b32_e32 v18, v38, v18, vcc
	v_cvt_pk_f16_f32 v14, v18, v14
	v_or_b32_e32 v18, v30, v25
	v_mov_b32_e32 v19, v9
	v_lshlrev_b64 v[18:19], 7, v[18:19]
	v_cndmask_b32_e32 v15, v41, v15, vcc
	v_lshl_add_u64 v[18:19], v[12:13], 0, v[18:19]
	v_cvt_pk_f16_f32 v15, v32, v15
	v_lshl_add_u64 v[18:19], v[18:19], 0, v[8:9]
	global_store_dwordx2 v[18:19], v[14:15], off
	v_pk_mul_f32 v[14:15], v[60:61], s[4:5] op_sel_hi:[1,0]
	v_pk_mul_f32 v[18:19], v[58:59], s[4:5] op_sel_hi:[1,0]
	v_cndmask_b32_e64 v32, v60, v14, s[0:1]
	v_cndmask_b32_e64 v14, v59, v19, s[0:1]
	v_cndmask_b32_e64 v18, v58, v18, s[0:1]
	v_cvt_pk_f16_f32 v14, v18, v14
	v_or_b32_e32 v18, v31, v25
	v_mov_b32_e32 v19, v9
	v_lshlrev_b64 v[18:19], 7, v[18:19]
	v_cndmask_b32_e64 v15, v61, v15, s[0:1]
	v_lshl_add_u64 v[18:19], v[10:11], 0, v[18:19]
	v_cvt_pk_f16_f32 v15, v32, v15
	v_lshl_add_u64 v[18:19], v[18:19], 0, v[22:23]
	global_store_dwordx2 v[18:19], v[14:15], off
	v_pk_mul_f32 v[14:15], v[28:29], s[4:5] op_sel_hi:[1,0]
	v_pk_mul_f32 v[18:19], v[26:27], s[4:5] op_sel_hi:[1,0]
	v_cndmask_b32_e64 v28, v28, v14, s[2:3]
	v_cndmask_b32_e64 v14, v27, v19, s[2:3]
	v_cndmask_b32_e64 v18, v26, v18, s[2:3]
	v_cvt_pk_f16_f32 v14, v18, v14
	v_or_b32_e32 v18, v24, v25
	v_mov_b32_e32 v19, v9
	v_lshlrev_b64 v[18:19], 7, v[18:19]
	v_cndmask_b32_e64 v15, v29, v15, s[2:3]
	v_lshl_add_u64 v[18:19], v[16:17], 0, v[18:19]
	v_cvt_pk_f16_f32 v15, v28, v15
	v_lshl_add_u64 v[18:19], v[18:19], 0, v[20:21]
	global_store_dwordx2 v[18:19], v[14:15], off
	v_pk_mul_f32 v[14:15], v[48:49], s[4:5] op_sel_hi:[1,0]
	v_pk_mul_f32 v[18:19], v[46:47], s[4:5] op_sel_hi:[1,0]
	v_or_b32_e32 v25, 32, v63
	v_cndmask_b32_e32 v26, v48, v14, vcc
	v_cndmask_b32_e32 v14, v47, v19, vcc
	v_cndmask_b32_e32 v18, v46, v18, vcc
	v_cvt_pk_f16_f32 v14, v18, v14
	v_or_b32_e32 v18, v30, v25
	v_mov_b32_e32 v19, v9
	v_lshlrev_b64 v[18:19], 7, v[18:19]
	v_cndmask_b32_e32 v15, v49, v15, vcc
	v_lshl_add_u64 v[18:19], v[12:13], 0, v[18:19]
	v_cvt_pk_f16_f32 v15, v26, v15
	v_lshl_add_u64 v[18:19], v[18:19], 0, v[8:9]
	global_store_dwordx2 v[18:19], v[14:15], off
	v_pk_mul_f32 v[14:15], v[52:53], s[4:5] op_sel_hi:[1,0]
	v_pk_mul_f32 v[18:19], v[50:51], s[4:5] op_sel_hi:[1,0]
	v_cndmask_b32_e64 v26, v52, v14, s[0:1]
	v_cndmask_b32_e64 v14, v51, v19, s[0:1]
	v_cndmask_b32_e64 v18, v50, v18, s[0:1]
	v_cvt_pk_f16_f32 v14, v18, v14
	v_or_b32_e32 v18, v31, v25
	v_mov_b32_e32 v19, v9
	v_lshlrev_b64 v[18:19], 7, v[18:19]
	v_cndmask_b32_e64 v15, v53, v15, s[0:1]
	v_lshl_add_u64 v[18:19], v[10:11], 0, v[18:19]
	v_cvt_pk_f16_f32 v15, v26, v15
	v_lshl_add_u64 v[18:19], v[18:19], 0, v[22:23]
	global_store_dwordx2 v[18:19], v[14:15], off
	v_pk_mul_f32 v[14:15], v[44:45], s[4:5] op_sel_hi:[1,0]
	v_pk_mul_f32 v[18:19], v[42:43], s[4:5] op_sel_hi:[1,0]
	v_cndmask_b32_e64 v26, v44, v14, s[2:3]
	v_cndmask_b32_e64 v14, v43, v19, s[2:3]
	v_cndmask_b32_e64 v18, v42, v18, s[2:3]
	v_cvt_pk_f16_f32 v14, v18, v14
	v_or_b32_e32 v18, v24, v25
	v_mov_b32_e32 v19, v9
	v_lshlrev_b64 v[18:19], 7, v[18:19]
	v_cndmask_b32_e64 v15, v45, v15, s[2:3]
	v_lshl_add_u64 v[18:19], v[16:17], 0, v[18:19]
	v_cvt_pk_f16_f32 v15, v26, v15
	v_lshl_add_u64 v[18:19], v[18:19], 0, v[20:21]
	global_store_dwordx2 v[18:19], v[14:15], off
	v_pk_mul_f32 v[14:15], v[56:57], s[4:5] op_sel_hi:[1,0]
	v_pk_mul_f32 v[18:19], v[54:55], s[4:5] op_sel_hi:[1,0]
	v_or_b32_e32 v25, 48, v63
	v_cndmask_b32_e32 v26, v56, v14, vcc
	v_cndmask_b32_e32 v14, v55, v19, vcc
	v_cndmask_b32_e32 v18, v54, v18, vcc
	v_cvt_pk_f16_f32 v14, v18, v14
	v_or_b32_e32 v18, v30, v25
	v_mov_b32_e32 v19, v9
	v_lshlrev_b64 v[18:19], 7, v[18:19]
	v_cndmask_b32_e32 v15, v57, v15, vcc
	v_lshl_add_u64 v[12:13], v[12:13], 0, v[18:19]
	v_cvt_pk_f16_f32 v15, v26, v15
	v_lshl_add_u64 v[12:13], v[12:13], 0, v[8:9]
	global_store_dwordx2 v[12:13], v[14:15], off
	v_pk_mul_f32 v[12:13], v[6:7], s[4:5] op_sel_hi:[1,0]
	v_pk_mul_f32 v[14:15], v[4:5], s[4:5] op_sel_hi:[1,0]
	v_cndmask_b32_e64 v7, v7, v13, s[0:1]
	v_cndmask_b32_e64 v6, v6, v12, s[0:1]
	v_cndmask_b32_e64 v5, v5, v15, s[0:1]
	v_cndmask_b32_e64 v4, v4, v14, s[0:1]
	v_or_b32_e32 v8, v31, v25
	v_cvt_pk_f16_f32 v4, v4, v5
	v_cvt_pk_f16_f32 v5, v6, v7
	v_lshlrev_b64 v[6:7], 7, v[8:9]
	v_lshl_add_u64 v[6:7], v[10:11], 0, v[6:7]
	v_lshl_add_u64 v[6:7], v[6:7], 0, v[22:23]
	global_store_dwordx2 v[6:7], v[4:5], off
	v_pk_mul_f32 v[4:5], v[2:3], s[4:5] op_sel_hi:[1,0]
	v_pk_mul_f32 v[6:7], v[0:1], s[4:5] op_sel_hi:[1,0]
	v_cndmask_b32_e64 v3, v3, v5, s[2:3]
	v_cndmask_b32_e64 v2, v2, v4, s[2:3]
	v_cndmask_b32_e64 v1, v1, v7, s[2:3]
	v_cndmask_b32_e64 v0, v0, v6, s[2:3]
	v_or_b32_e32 v8, v24, v25
	v_cvt_pk_f16_f32 v0, v0, v1
	v_cvt_pk_f16_f32 v1, v2, v3
	v_lshlrev_b64 v[2:3], 7, v[8:9]
	v_lshl_add_u64 v[2:3], v[16:17], 0, v[2:3]
	v_lshl_add_u64 v[2:3], v[2:3], 0, v[20:21]
	global_store_dwordx2 v[2:3], v[0:1], off
	s_endpgm
	s_endpgm
	s_endpgm
	s_endpgm
	s_endpgm
	s_endpgm
	s_endpgm
	s_endpgm
	s_endpgm
	s_endpgm
	s_endpgm
	s_endpgm
	s_endpgm
	s_endpgm
	s_endpgm
	s_endpgm
	s_endpgm
	s_endpgm
	s_endpgm
	s_endpgm
	s_endpgm
	s_endpgm
	s_endpgm
	s_endpgm
	s_endpgm
	s_endpgm
	s_endpgm
	s_endpgm
	s_endpgm
	s_endpgm
	s_endpgm
	s_endpgm
	s_endpgm
	s_endpgm
	s_endpgm
	s_endpgm
	s_endpgm
	s_endpgm
	s_endpgm
	s_endpgm
	s_endpgm
	s_endpgm
	s_endpgm
	s_endpgm
	s_endpgm
	s_endpgm
